# grid barrier: the XCD leader releases its XCD's generation word before invalidating its own caches
# speedup vs baseline: 1.0010x; 1.0010x over previous
.LBB0_155:
	s_or_b64 exec, exec, s[0:1]
	v_mov_b32_e32 v1, s21
	v_add_co_u32_e32 v2, vcc, 0x2000, v1
	v_mov_b32_e32 v1, s20
	s_nop 0
	v_addc_co_u32_e32 v3, vcc, 0, v1, vcc
	v_mov_b32_e32 v1, 1
	s_waitcnt vmcnt(0) lgkmcnt(0)
	flat_atomic_add v[2:3], v1 offset:1024
	buffer_inv sc1
	s_waitcnt vmcnt(0)

.LBB0_158:
	s_or_b64 exec, exec, s[2:3]
	v_mov_b32_e32 v1, s25
	v_add_co_u32_e32 v4, vcc, 0x2000, v1
	v_mov_b32_e32 v1, s24
	s_nop 0
	v_addc_co_u32_e32 v5, vcc, 0, v1, vcc
	s_waitcnt vmcnt(0) lgkmcnt(0)
	flat_atomic_add v[4:5], v211 offset:1024
	buffer_inv sc1
	s_waitcnt vmcnt(0)
